# v29
# speedup vs baseline: 1.0078x; 1.0078x over previous
.LBB0_9:
	s_setprio 3
	s_waitcnt vmcnt(15)
	v_cvt_pk_bf16_f32 v2, v34, v35
	v_cvt_pk_bf16_f32 v3, v36, v37
	s_waitcnt vmcnt(11)
	v_cvt_pk_bf16_f32 v10, v50, v51
	v_cvt_pk_bf16_f32 v11, v52, v53
	v_cvt_pk_bf16_f32 v4, v38, v39
	v_cvt_pk_bf16_f32 v5, v40, v41
	ds_write2_b64 v212, v[2:3], v[10:11] offset1:68
	s_waitcnt vmcnt(10)
	v_cvt_pk_bf16_f32 v2, v54, v55
	v_cvt_pk_bf16_f32 v3, v56, v57
	v_cvt_pk_bf16_f32 v6, v42, v43
	v_cvt_pk_bf16_f32 v7, v44, v45
	ds_write2_b64 v215, v[4:5], v[2:3] offset0:16 offset1:84
	s_waitcnt vmcnt(9)
	v_cvt_pk_bf16_f32 v2, v58, v59
	v_cvt_pk_bf16_f32 v3, v60, v61
	v_cvt_pk_bf16_f32 v8, v46, v47
	v_cvt_pk_bf16_f32 v9, v48, v49
	ds_write2_b64 v216, v[6:7], v[2:3] offset0:32 offset1:100
	s_waitcnt vmcnt(8)
	v_cvt_pk_bf16_f32 v2, v62, v63
	v_cvt_pk_bf16_f32 v3, v64, v65
	ds_write2_b64 v217, v[8:9], v[2:3] offset0:48 offset1:116
	s_waitcnt vmcnt(7)
	v_cvt_pk_bf16_f32 v2, v66, v67
	v_cvt_pk_bf16_f32 v3, v68, v69
	s_waitcnt vmcnt(3)
	v_cvt_pk_bf16_f32 v10, v82, v83
	v_cvt_pk_bf16_f32 v11, v84, v85
	v_cvt_pk_bf16_f32 v4, v70, v71
	v_cvt_pk_bf16_f32 v5, v72, v73
	ds_write2_b64 v212, v[2:3], v[10:11] offset0:136 offset1:204
	s_waitcnt vmcnt(2)
	v_cvt_pk_bf16_f32 v2, v86, v87
	v_cvt_pk_bf16_f32 v3, v88, v89
	v_cvt_pk_bf16_f32 v6, v74, v75
	v_cvt_pk_bf16_f32 v7, v76, v77
	ds_write2_b64 v215, v[4:5], v[2:3] offset0:152 offset1:220
	s_waitcnt vmcnt(1)
	v_cvt_pk_bf16_f32 v2, v90, v91
	v_cvt_pk_bf16_f32 v3, v92, v93
	v_cvt_pk_bf16_f32 v8, v78, v79
	v_cvt_pk_bf16_f32 v9, v80, v81
	ds_write2_b64 v216, v[6:7], v[2:3] offset0:168 offset1:236
	s_waitcnt vmcnt(0)
	v_cvt_pk_bf16_f32 v2, v94, v95
	v_cvt_pk_bf16_f32 v3, v96, v97
	ds_write2_b64 v217, v[8:9], v[2:3] offset0:184 offset1:252
	s_add_i32 s26, s35, 8
	s_cmpk_lt_i32 s26, 0x80
	s_mov_b64 s[24:25], -1
	s_cbranch_scc1 .LBB0_15
	global_load_dwordx4 v[26:29], v[134:135], off offset:16
	global_load_dwordx4 v[30:33], v[134:135], off
	global_load_dwordx4 v[18:21], v[134:135], off offset:144
	global_load_dwordx4 v[22:25], v[134:135], off offset:128
	global_load_dwordx4 v[10:13], v[134:135], off offset:272
	global_load_dwordx4 v[14:17], v[134:135], off offset:256
	global_load_dwordx4 v[2:5], v[134:135], off offset:400
	global_load_dwordx4 v[6:9], v[134:135], off offset:384
	s_mov_b64 s[24:25], 0

.LBB0_17:
	s_setprio 0
	s_waitcnt lgkmcnt(0)
	s_ashr_i32 s27, s35, 5
	s_cmp_eq_u32 s27, s34
	s_cbranch_scc1 .LBB0_37
	ds_bpermute_b32 v98, v208, v218
	v_max_f32_e32 v99, v218, v218
	v_mov_b32_e32 v101, 0
	v_mov_b32_e32 v102, 0
	v_mov_b32_e32 v103, 0
	s_waitcnt lgkmcnt(0)
	v_max_f32_e32 v98, v98, v98
	v_max_f32_e32 v98, v99, v98
	ds_bpermute_b32 v99, v207, v98
	v_mov_b32_e32 v104, 0
	v_mov_b32_e32 v105, 0
	v_mov_b32_e32 v106, 0
	s_lshl_b32 s24, s34, 3
	s_waitcnt lgkmcnt(0)
	v_max_f32_e32 v99, v99, v99
	v_max_f32_e32 v98, v98, v99
	ds_bpermute_b32 v100, v206, v98
	s_add_i32 s24, s24, s31
	s_mul_i32 s28, s24, 0x210
	v_mov_b32_e32 v99, 0
	s_add_i32 s28, s28, 0x23440
	s_waitcnt lgkmcnt(0)
	v_max_f32_e32 v100, v100, v100
	v_max_f32_e32 v98, v98, v100
	ds_bpermute_b32 v100, v205, v98
	v_add_u32_e32 v111, s28, v203
	s_waitcnt lgkmcnt(0)
	v_max_f32_e32 v100, v100, v100
	v_max_f32_e32 v98, v98, v100
	v_sub_f32_e32 v100, v218, v98
	v_exp_f32_e32 v100, v100
	s_nop 0
	v_mul_f32_e32 v107, v219, v100
	v_pk_mul_f32 v[108:109], v[100:101], v[198:199] op_sel_hi:[0,1]
	s_nop 0
	v_mov_b32_dpp v101, v107 row_shr:1 row_mask:0xf bank_mask:0xf
	v_fmac_f32_e32 v101, v219, v100
	v_mov_b32_dpp v102, v108 row_shr:1 row_mask:0xf bank_mask:0xf
	v_mov_b32_dpp v103, v109 row_shr:1 row_mask:0xf bank_mask:0xf
	v_pk_fma_f32 v[102:103], v[100:101], v[198:199], v[102:103] op_sel_hi:[0,1,1]
	v_mov_b32_e32 v107, 0
	v_add_f32_dpp v101, v101, v101 row_shr:2 row_mask:0xf bank_mask:0xf bound_ctrl:1
	v_mov_b32_dpp v104, v102 row_shr:2 row_mask:0xf bank_mask:0xf
	v_mov_b32_dpp v105, v103 row_shr:2 row_mask:0xf bank_mask:0xf
	v_pk_add_f32 v[102:103], v[102:103], v[104:105]
	v_mov_b32_e32 v108, 0
	v_mov_b32_e32 v109, 0
	v_mov_b32_dpp v106, v102 row_shr:4 row_mask:0xf bank_mask:0xf
	v_mov_b32_dpp v107, v103 row_shr:4 row_mask:0xf bank_mask:0xf
	v_pk_add_f32 v[102:103], v[102:103], v[106:107]
	v_pk_mul_f32 v[106:107], v[100:101], v[196:197] op_sel_hi:[0,1]
	v_add_f32_dpp v110, v101, v101 row_shr:4 row_mask:0xf bank_mask:0xf bound_ctrl:1
	v_mov_b32_e32 v104, 0
	v_mov_b32_dpp v108, v106 row_shr:1 row_mask:0xf bank_mask:0xf
	v_mov_b32_dpp v109, v107 row_shr:1 row_mask:0xf bank_mask:0xf
	v_pk_fma_f32 v[106:107], v[100:101], v[196:197], v[108:109] op_sel_hi:[0,1,1]
	v_mov_b32_e32 v108, 0
	v_mov_b32_e32 v109, 0
	v_mov_b32_e32 v105, 0
	v_mov_b32_dpp v108, v106 row_shr:2 row_mask:0xf bank_mask:0xf
	v_mov_b32_dpp v109, v107 row_shr:2 row_mask:0xf bank_mask:0xf
	v_pk_add_f32 v[106:107], v[106:107], v[108:109]
	v_mov_b32_e32 v108, 0
	v_mov_b32_e32 v109, 0
	v_mov_b32_dpp v99, v110 row_shr:8 row_mask:0xf bank_mask:0xf
	v_mov_b32_dpp v108, v106 row_shr:4 row_mask:0xf bank_mask:0xf
	v_mov_b32_dpp v109, v107 row_shr:4 row_mask:0xf bank_mask:0xf
	v_pk_add_f32 v[106:107], v[106:107], v[108:109]
	v_mov_b32_e32 v108, 0
	v_mov_b32_e32 v109, 0
	v_mov_b32_dpp v104, v102 row_shr:8 row_mask:0xf bank_mask:0xf
	v_mov_b32_dpp v105, v103 row_shr:8 row_mask:0xf bank_mask:0xf
	v_mov_b32_dpp v108, v106 row_shr:8 row_mask:0xf bank_mask:0xf
	v_mov_b32_dpp v109, v107 row_shr:8 row_mask:0xf bank_mask:0xf
	s_and_saveexec_b64 s[24:25], s[6:7]
	v_pk_add_f32 v[106:107], v[106:107], v[108:109]
	v_pk_add_f32 v[104:105], v[102:103], v[104:105]
	ds_write_b128 v111, v[104:107]
	s_or_b64 exec, exec, s[24:25]
	v_mov_b32_e32 v101, v100
	v_pk_mul_f32 v[102:103], v[100:101], v[194:195]
	v_mov_b32_e32 v104, 0
	v_mov_b32_e32 v105, 0
	v_pk_mul_f32 v[106:107], v[100:101], v[192:193]
	v_mov_b32_e32 v108, 0
	v_mov_b32_e32 v109, 0
	v_mov_b32_dpp v104, v102 row_shr:1 row_mask:0xf bank_mask:0xf
	v_mov_b32_dpp v105, v103 row_shr:1 row_mask:0xf bank_mask:0xf
	v_mov_b32_dpp v108, v106 row_shr:1 row_mask:0xf bank_mask:0xf
	v_mov_b32_dpp v109, v107 row_shr:1 row_mask:0xf bank_mask:0xf
	v_pk_fma_f32 v[102:103], v[100:101], v[194:195], v[104:105]
	v_mov_b32_e32 v104, 0
	v_mov_b32_e32 v105, 0
	v_pk_fma_f32 v[106:107], v[100:101], v[192:193], v[108:109]
	v_mov_b32_e32 v108, 0
	v_mov_b32_e32 v109, 0
	v_mov_b32_dpp v104, v102 row_shr:2 row_mask:0xf bank_mask:0xf
	v_mov_b32_dpp v105, v103 row_shr:2 row_mask:0xf bank_mask:0xf
	v_mov_b32_dpp v108, v106 row_shr:2 row_mask:0xf bank_mask:0xf
	v_mov_b32_dpp v109, v107 row_shr:2 row_mask:0xf bank_mask:0xf
	v_pk_add_f32 v[102:103], v[102:103], v[104:105]
	v_mov_b32_e32 v104, 0
	v_mov_b32_e32 v105, 0
	v_pk_add_f32 v[106:107], v[106:107], v[108:109]
	v_mov_b32_e32 v108, 0
	v_mov_b32_e32 v109, 0
	v_mov_b32_dpp v104, v102 row_shr:4 row_mask:0xf bank_mask:0xf
	v_mov_b32_dpp v105, v103 row_shr:4 row_mask:0xf bank_mask:0xf
	v_mov_b32_dpp v108, v106 row_shr:4 row_mask:0xf bank_mask:0xf
	v_mov_b32_dpp v109, v107 row_shr:4 row_mask:0xf bank_mask:0xf
	v_pk_add_f32 v[102:103], v[102:103], v[104:105]
	v_mov_b32_e32 v104, 0
	v_mov_b32_e32 v105, 0
	v_pk_add_f32 v[106:107], v[106:107], v[108:109]
	v_mov_b32_e32 v108, 0
	v_mov_b32_e32 v109, 0
	v_mov_b32_dpp v104, v102 row_shr:8 row_mask:0xf bank_mask:0xf
	v_mov_b32_dpp v105, v103 row_shr:8 row_mask:0xf bank_mask:0xf
	v_mov_b32_dpp v108, v106 row_shr:8 row_mask:0xf bank_mask:0xf
	v_mov_b32_dpp v109, v107 row_shr:8 row_mask:0xf bank_mask:0xf
	s_and_saveexec_b64 s[24:25], s[6:7]
	v_pk_add_f32 v[106:107], v[106:107], v[108:109]
	v_pk_add_f32 v[104:105], v[102:103], v[104:105]
	ds_write_b128 v111, v[104:107] offset:64
	s_or_b64 exec, exec, s[24:25]
	v_pk_mul_f32 v[102:103], v[100:101], v[190:191]
	v_mov_b32_e32 v104, 0
	v_mov_b32_e32 v105, 0
	v_pk_mul_f32 v[106:107], v[100:101], v[188:189]
	v_mov_b32_e32 v108, 0
	v_mov_b32_e32 v109, 0
	v_mov_b32_dpp v104, v102 row_shr:1 row_mask:0xf bank_mask:0xf
	v_mov_b32_dpp v105, v103 row_shr:1 row_mask:0xf bank_mask:0xf
	v_mov_b32_dpp v108, v106 row_shr:1 row_mask:0xf bank_mask:0xf
	v_mov_b32_dpp v109, v107 row_shr:1 row_mask:0xf bank_mask:0xf
	v_pk_fma_f32 v[102:103], v[100:101], v[190:191], v[104:105]
	v_mov_b32_e32 v104, 0
	v_mov_b32_e32 v105, 0
	v_pk_fma_f32 v[106:107], v[100:101], v[188:189], v[108:109]
	v_mov_b32_e32 v108, 0
	v_mov_b32_e32 v109, 0
	v_mov_b32_dpp v104, v102 row_shr:2 row_mask:0xf bank_mask:0xf
	v_mov_b32_dpp v105, v103 row_shr:2 row_mask:0xf bank_mask:0xf
	v_mov_b32_dpp v108, v106 row_shr:2 row_mask:0xf bank_mask:0xf
	v_mov_b32_dpp v109, v107 row_shr:2 row_mask:0xf bank_mask:0xf
	v_pk_add_f32 v[102:103], v[102:103], v[104:105]
	v_mov_b32_e32 v104, 0
	v_mov_b32_e32 v105, 0
	v_pk_add_f32 v[106:107], v[106:107], v[108:109]
	v_mov_b32_e32 v108, 0
	v_mov_b32_e32 v109, 0
	v_mov_b32_dpp v104, v102 row_shr:4 row_mask:0xf bank_mask:0xf
	v_mov_b32_dpp v105, v103 row_shr:4 row_mask:0xf bank_mask:0xf
	v_mov_b32_dpp v108, v106 row_shr:4 row_mask:0xf bank_mask:0xf
	v_mov_b32_dpp v109, v107 row_shr:4 row_mask:0xf bank_mask:0xf
	v_pk_add_f32 v[102:103], v[102:103], v[104:105]
	v_mov_b32_e32 v104, 0
	v_mov_b32_e32 v105, 0
	v_pk_add_f32 v[106:107], v[106:107], v[108:109]
	v_mov_b32_e32 v108, 0
	v_mov_b32_e32 v109, 0
	v_mov_b32_dpp v104, v102 row_shr:8 row_mask:0xf bank_mask:0xf
	v_mov_b32_dpp v105, v103 row_shr:8 row_mask:0xf bank_mask:0xf
	v_mov_b32_dpp v108, v106 row_shr:8 row_mask:0xf bank_mask:0xf
	v_mov_b32_dpp v109, v107 row_shr:8 row_mask:0xf bank_mask:0xf
	s_and_saveexec_b64 s[24:25], s[6:7]
	v_pk_add_f32 v[106:107], v[106:107], v[108:109]
	v_pk_add_f32 v[104:105], v[102:103], v[104:105]
	ds_write_b128 v111, v[104:107] offset:128
	s_or_b64 exec, exec, s[24:25]
	v_pk_mul_f32 v[102:103], v[100:101], v[186:187]
	v_mov_b32_e32 v104, 0
	v_mov_b32_e32 v105, 0
	v_pk_mul_f32 v[106:107], v[100:101], v[184:185]
	v_mov_b32_e32 v108, 0
	v_mov_b32_e32 v109, 0
	v_mov_b32_dpp v104, v102 row_shr:1 row_mask:0xf bank_mask:0xf
	v_mov_b32_dpp v105, v103 row_shr:1 row_mask:0xf bank_mask:0xf
	v_mov_b32_dpp v108, v106 row_shr:1 row_mask:0xf bank_mask:0xf
	v_mov_b32_dpp v109, v107 row_shr:1 row_mask:0xf bank_mask:0xf
	v_pk_fma_f32 v[102:103], v[100:101], v[186:187], v[104:105]
	v_mov_b32_e32 v104, 0
	v_mov_b32_e32 v105, 0
	v_pk_fma_f32 v[106:107], v[100:101], v[184:185], v[108:109]
	v_mov_b32_e32 v108, 0
	v_mov_b32_e32 v109, 0
	v_mov_b32_dpp v104, v102 row_shr:2 row_mask:0xf bank_mask:0xf
	v_mov_b32_dpp v105, v103 row_shr:2 row_mask:0xf bank_mask:0xf
	v_mov_b32_dpp v108, v106 row_shr:2 row_mask:0xf bank_mask:0xf
	v_mov_b32_dpp v109, v107 row_shr:2 row_mask:0xf bank_mask:0xf
	v_pk_add_f32 v[102:103], v[102:103], v[104:105]
	v_mov_b32_e32 v104, 0
	v_mov_b32_e32 v105, 0
	v_pk_add_f32 v[106:107], v[106:107], v[108:109]
	v_mov_b32_e32 v108, 0
	v_mov_b32_e32 v109, 0
	v_mov_b32_dpp v104, v102 row_shr:4 row_mask:0xf bank_mask:0xf
	v_mov_b32_dpp v105, v103 row_shr:4 row_mask:0xf bank_mask:0xf
	v_mov_b32_dpp v108, v106 row_shr:4 row_mask:0xf bank_mask:0xf
	v_mov_b32_dpp v109, v107 row_shr:4 row_mask:0xf bank_mask:0xf
	v_pk_add_f32 v[102:103], v[102:103], v[104:105]
	v_mov_b32_e32 v104, 0
	v_mov_b32_e32 v105, 0
	v_pk_add_f32 v[106:107], v[106:107], v[108:109]
	v_mov_b32_e32 v108, 0
	v_mov_b32_e32 v109, 0
	v_mov_b32_dpp v104, v102 row_shr:8 row_mask:0xf bank_mask:0xf
	v_mov_b32_dpp v105, v103 row_shr:8 row_mask:0xf bank_mask:0xf
	v_mov_b32_dpp v108, v106 row_shr:8 row_mask:0xf bank_mask:0xf
	v_mov_b32_dpp v109, v107 row_shr:8 row_mask:0xf bank_mask:0xf
	s_and_saveexec_b64 s[24:25], s[6:7]
	v_pk_add_f32 v[106:107], v[106:107], v[108:109]
	v_pk_add_f32 v[104:105], v[102:103], v[104:105]
	ds_write_b128 v111, v[104:107] offset:192
	s_or_b64 exec, exec, s[24:25]
	v_pk_mul_f32 v[102:103], v[100:101], v[182:183]
	v_mov_b32_e32 v104, 0
	v_mov_b32_e32 v105, 0
	v_pk_mul_f32 v[106:107], v[100:101], v[180:181]
	v_mov_b32_e32 v108, 0
	v_mov_b32_e32 v109, 0
	v_mov_b32_dpp v104, v102 row_shr:1 row_mask:0xf bank_mask:0xf
	v_mov_b32_dpp v105, v103 row_shr:1 row_mask:0xf bank_mask:0xf
	v_mov_b32_dpp v108, v106 row_shr:1 row_mask:0xf bank_mask:0xf
	v_mov_b32_dpp v109, v107 row_shr:1 row_mask:0xf bank_mask:0xf
	v_pk_fma_f32 v[102:103], v[100:101], v[182:183], v[104:105]
	v_mov_b32_e32 v104, 0
	v_mov_b32_e32 v105, 0
	v_pk_fma_f32 v[106:107], v[100:101], v[180:181], v[108:109]
	v_mov_b32_e32 v108, 0
	v_mov_b32_e32 v109, 0
	v_mov_b32_dpp v104, v102 row_shr:2 row_mask:0xf bank_mask:0xf
	v_mov_b32_dpp v105, v103 row_shr:2 row_mask:0xf bank_mask:0xf
	v_mov_b32_dpp v108, v106 row_shr:2 row_mask:0xf bank_mask:0xf
	v_mov_b32_dpp v109, v107 row_shr:2 row_mask:0xf bank_mask:0xf
	v_pk_add_f32 v[102:103], v[102:103], v[104:105]
	v_mov_b32_e32 v104, 0
	v_mov_b32_e32 v105, 0
	v_pk_add_f32 v[106:107], v[106:107], v[108:109]
	v_mov_b32_e32 v108, 0
	v_mov_b32_e32 v109, 0
	v_mov_b32_dpp v104, v102 row_shr:4 row_mask:0xf bank_mask:0xf
	v_mov_b32_dpp v105, v103 row_shr:4 row_mask:0xf bank_mask:0xf
	v_mov_b32_dpp v108, v106 row_shr:4 row_mask:0xf bank_mask:0xf
	v_mov_b32_dpp v109, v107 row_shr:4 row_mask:0xf bank_mask:0xf
	v_pk_add_f32 v[102:103], v[102:103], v[104:105]
	v_mov_b32_e32 v104, 0
	v_mov_b32_e32 v105, 0
	v_pk_add_f32 v[106:107], v[106:107], v[108:109]
	v_mov_b32_e32 v108, 0
	v_mov_b32_e32 v109, 0
	v_mov_b32_dpp v104, v102 row_shr:8 row_mask:0xf bank_mask:0xf
	v_mov_b32_dpp v105, v103 row_shr:8 row_mask:0xf bank_mask:0xf
	v_mov_b32_dpp v108, v106 row_shr:8 row_mask:0xf bank_mask:0xf
	v_mov_b32_dpp v109, v107 row_shr:8 row_mask:0xf bank_mask:0xf
	s_and_saveexec_b64 s[24:25], s[6:7]
	v_pk_add_f32 v[106:107], v[106:107], v[108:109]
	v_pk_add_f32 v[104:105], v[102:103], v[104:105]
	ds_write_b128 v111, v[104:107] offset:256
	s_or_b64 exec, exec, s[24:25]
	v_pk_mul_f32 v[102:103], v[100:101], v[178:179]
	v_mov_b32_e32 v104, 0
	v_mov_b32_e32 v105, 0
	v_pk_mul_f32 v[106:107], v[100:101], v[168:169]
	v_mov_b32_e32 v108, 0
	v_mov_b32_e32 v109, 0
	v_mov_b32_dpp v104, v102 row_shr:1 row_mask:0xf bank_mask:0xf
	v_mov_b32_dpp v105, v103 row_shr:1 row_mask:0xf bank_mask:0xf
	v_mov_b32_dpp v108, v106 row_shr:1 row_mask:0xf bank_mask:0xf
	v_mov_b32_dpp v109, v107 row_shr:1 row_mask:0xf bank_mask:0xf
	v_pk_fma_f32 v[102:103], v[100:101], v[178:179], v[104:105]
	v_mov_b32_e32 v104, 0
	v_mov_b32_e32 v105, 0
	v_pk_fma_f32 v[106:107], v[100:101], v[168:169], v[108:109]
	v_mov_b32_e32 v108, 0
	v_mov_b32_e32 v109, 0
	v_mov_b32_dpp v104, v102 row_shr:2 row_mask:0xf bank_mask:0xf
	v_mov_b32_dpp v105, v103 row_shr:2 row_mask:0xf bank_mask:0xf
	v_mov_b32_dpp v108, v106 row_shr:2 row_mask:0xf bank_mask:0xf
	v_mov_b32_dpp v109, v107 row_shr:2 row_mask:0xf bank_mask:0xf
	v_pk_add_f32 v[102:103], v[102:103], v[104:105]
	v_mov_b32_e32 v104, 0
	v_mov_b32_e32 v105, 0
	v_pk_add_f32 v[106:107], v[106:107], v[108:109]
	v_mov_b32_e32 v108, 0
	v_mov_b32_e32 v109, 0
	v_mov_b32_dpp v104, v102 row_shr:4 row_mask:0xf bank_mask:0xf
	v_mov_b32_dpp v105, v103 row_shr:4 row_mask:0xf bank_mask:0xf
	v_mov_b32_dpp v108, v106 row_shr:4 row_mask:0xf bank_mask:0xf
	v_mov_b32_dpp v109, v107 row_shr:4 row_mask:0xf bank_mask:0xf
	v_pk_add_f32 v[102:103], v[102:103], v[104:105]
	v_mov_b32_e32 v104, 0
	v_mov_b32_e32 v105, 0
	v_pk_add_f32 v[106:107], v[106:107], v[108:109]
	v_mov_b32_e32 v108, 0
	v_mov_b32_e32 v109, 0
	v_mov_b32_dpp v104, v102 row_shr:8 row_mask:0xf bank_mask:0xf
	v_mov_b32_dpp v105, v103 row_shr:8 row_mask:0xf bank_mask:0xf
	v_mov_b32_dpp v108, v106 row_shr:8 row_mask:0xf bank_mask:0xf
	v_mov_b32_dpp v109, v107 row_shr:8 row_mask:0xf bank_mask:0xf
	s_and_saveexec_b64 s[24:25], s[6:7]
	v_pk_add_f32 v[106:107], v[106:107], v[108:109]
	v_pk_add_f32 v[104:105], v[102:103], v[104:105]
	ds_write_b128 v111, v[104:107] offset:320
	s_or_b64 exec, exec, s[24:25]
	v_pk_mul_f32 v[102:103], v[100:101], v[150:151]
	v_mov_b32_e32 v104, 0
	v_mov_b32_e32 v105, 0
	v_pk_mul_f32 v[106:107], v[100:101], v[140:141]
	v_mov_b32_e32 v108, 0
	v_mov_b32_e32 v109, 0
	v_mov_b32_dpp v104, v102 row_shr:1 row_mask:0xf bank_mask:0xf
	v_mov_b32_dpp v105, v103 row_shr:1 row_mask:0xf bank_mask:0xf
	v_mov_b32_dpp v108, v106 row_shr:1 row_mask:0xf bank_mask:0xf
	v_mov_b32_dpp v109, v107 row_shr:1 row_mask:0xf bank_mask:0xf
	v_pk_fma_f32 v[102:103], v[100:101], v[150:151], v[104:105]
	v_mov_b32_e32 v104, 0
	v_mov_b32_e32 v105, 0
	v_pk_fma_f32 v[106:107], v[100:101], v[140:141], v[108:109]
	v_mov_b32_e32 v108, 0
	v_mov_b32_e32 v109, 0
	v_mov_b32_dpp v104, v102 row_shr:2 row_mask:0xf bank_mask:0xf
	v_mov_b32_dpp v105, v103 row_shr:2 row_mask:0xf bank_mask:0xf
	v_mov_b32_dpp v108, v106 row_shr:2 row_mask:0xf bank_mask:0xf
	v_mov_b32_dpp v109, v107 row_shr:2 row_mask:0xf bank_mask:0xf
	v_pk_add_f32 v[102:103], v[102:103], v[104:105]
	v_mov_b32_e32 v104, 0
	v_mov_b32_e32 v105, 0
	v_pk_add_f32 v[106:107], v[106:107], v[108:109]
	v_mov_b32_e32 v108, 0
	v_mov_b32_e32 v109, 0
	v_mov_b32_dpp v104, v102 row_shr:4 row_mask:0xf bank_mask:0xf
	v_mov_b32_dpp v105, v103 row_shr:4 row_mask:0xf bank_mask:0xf
	v_mov_b32_dpp v108, v106 row_shr:4 row_mask:0xf bank_mask:0xf
	v_mov_b32_dpp v109, v107 row_shr:4 row_mask:0xf bank_mask:0xf
	v_pk_add_f32 v[102:103], v[102:103], v[104:105]
	v_mov_b32_e32 v104, 0
	v_mov_b32_e32 v105, 0
	v_pk_add_f32 v[106:107], v[106:107], v[108:109]
	v_mov_b32_e32 v108, 0
	v_mov_b32_e32 v109, 0
	v_mov_b32_dpp v104, v102 row_shr:8 row_mask:0xf bank_mask:0xf
	v_mov_b32_dpp v105, v103 row_shr:8 row_mask:0xf bank_mask:0xf
	v_mov_b32_dpp v108, v106 row_shr:8 row_mask:0xf bank_mask:0xf
	v_mov_b32_dpp v109, v107 row_shr:8 row_mask:0xf bank_mask:0xf
	s_and_saveexec_b64 s[24:25], s[6:7]
	v_pk_add_f32 v[106:107], v[106:107], v[108:109]
	v_pk_add_f32 v[104:105], v[102:103], v[104:105]
	ds_write_b128 v111, v[104:107] offset:384
	s_or_b64 exec, exec, s[24:25]
	v_pk_mul_f32 v[102:103], v[100:101], v[138:139]
	v_mov_b32_e32 v104, 0
	v_mov_b32_e32 v105, 0
	v_pk_mul_f32 v[106:107], v[100:101], v[136:137]
	v_mov_b32_e32 v108, 0
	v_mov_b32_e32 v109, 0
	v_mov_b32_dpp v104, v102 row_shr:1 row_mask:0xf bank_mask:0xf
	v_mov_b32_dpp v105, v103 row_shr:1 row_mask:0xf bank_mask:0xf
	v_mov_b32_dpp v108, v106 row_shr:1 row_mask:0xf bank_mask:0xf
	v_mov_b32_dpp v109, v107 row_shr:1 row_mask:0xf bank_mask:0xf
	v_pk_fma_f32 v[102:103], v[100:101], v[138:139], v[104:105]
	v_mov_b32_e32 v104, 0
	v_mov_b32_e32 v105, 0
	v_pk_fma_f32 v[100:101], v[100:101], v[136:137], v[108:109]
	v_mov_b32_e32 v106, 0
	v_mov_b32_e32 v107, 0
	v_mov_b32_dpp v104, v102 row_shr:2 row_mask:0xf bank_mask:0xf
	v_mov_b32_dpp v105, v103 row_shr:2 row_mask:0xf bank_mask:0xf
	v_mov_b32_dpp v106, v100 row_shr:2 row_mask:0xf bank_mask:0xf
	v_mov_b32_dpp v107, v101 row_shr:2 row_mask:0xf bank_mask:0xf
	v_pk_add_f32 v[102:103], v[102:103], v[104:105]
	v_mov_b32_e32 v104, 0
	v_mov_b32_e32 v105, 0
	v_pk_add_f32 v[100:101], v[100:101], v[106:107]
	v_mov_b32_e32 v106, 0
	v_mov_b32_e32 v107, 0
	v_mov_b32_dpp v104, v102 row_shr:4 row_mask:0xf bank_mask:0xf
	v_mov_b32_dpp v105, v103 row_shr:4 row_mask:0xf bank_mask:0xf
	v_mov_b32_dpp v106, v100 row_shr:4 row_mask:0xf bank_mask:0xf
	v_mov_b32_dpp v107, v101 row_shr:4 row_mask:0xf bank_mask:0xf
	v_pk_add_f32 v[102:103], v[102:103], v[104:105]
	v_mov_b32_e32 v104, 0
	v_mov_b32_e32 v105, 0
	v_pk_add_f32 v[100:101], v[100:101], v[106:107]
	v_mov_b32_e32 v106, 0
	v_mov_b32_e32 v107, 0
	v_mov_b32_dpp v104, v102 row_shr:8 row_mask:0xf bank_mask:0xf
	v_mov_b32_dpp v105, v103 row_shr:8 row_mask:0xf bank_mask:0xf
	v_mov_b32_dpp v106, v100 row_shr:8 row_mask:0xf bank_mask:0xf
	v_mov_b32_dpp v107, v101 row_shr:8 row_mask:0xf bank_mask:0xf
	s_and_saveexec_b64 s[24:25], s[6:7]
	v_pk_add_f32 v[106:107], v[100:101], v[106:107]
	v_pk_add_f32 v[104:105], v[102:103], v[104:105]
	ds_write_b128 v111, v[104:107] offset:448
	s_or_b64 exec, exec, s[24:25]
	s_and_saveexec_b64 s[24:25], s[4:5]
	v_add_f32_e32 v99, v110, v99
	v_mov_b32_e32 v100, s28
	ds_write_b64 v100, v[98:99] offset:512
	s_or_b64 exec, exec, s[24:25]
	v_mov_b32_e32 v218, 0xff800000
	v_mov_b32_e32 v219, 0
	v_mov_b32_e32 v198, 0
	v_mov_b32_e32 v199, 0
	v_mov_b32_e32 v196, 0
	v_mov_b32_e32 v197, 0
	v_mov_b32_e32 v194, 0
	v_mov_b32_e32 v195, 0
	v_mov_b32_e32 v192, 0
	v_mov_b32_e32 v193, 0
	v_mov_b32_e32 v190, 0
	v_mov_b32_e32 v191, 0
	v_mov_b32_e32 v188, 0
	v_mov_b32_e32 v189, 0
	v_mov_b32_e32 v186, 0
	v_mov_b32_e32 v187, 0
	v_mov_b32_e32 v184, 0
	v_mov_b32_e32 v185, 0
	v_mov_b32_e32 v182, 0
	v_mov_b32_e32 v183, 0
	v_mov_b32_e32 v180, 0
	v_mov_b32_e32 v181, 0
	v_mov_b32_e32 v178, 0
	v_mov_b32_e32 v179, 0
	v_mov_b32_e32 v168, 0
	v_mov_b32_e32 v169, 0
	v_mov_b32_e32 v150, 0
	v_mov_b32_e32 v151, 0
	v_mov_b32_e32 v140, 0
	v_mov_b32_e32 v141, 0
	v_mov_b32_e32 v138, 0
	v_mov_b32_e32 v139, 0
	v_mov_b32_e32 v136, 0
	v_mov_b32_e32 v137, 0
	s_waitcnt lgkmcnt(0)
	s_branch .Lp1_mfma
